# speedup vs baseline: 1.0089x; 1.0012x over previous
.Lep1_end:
	v_mov_b32_e32 v2, v0
	s_waitcnt lgkmcnt(0)
	s_barrier
	s_lshl_b32 s30, s36, 1
	v_ashrrev_i32_e32 v3, 5, v2
	v_lshlrev_b32_e32 v2, 4, v2
	v_and_b32_e32 v2, 0x1f0, v2
	v_min_i32_e32 v4, 0x53, v3
	v_lshl_or_b32 v4, v4, 9, v2
	v_min_i32_e32 v5, 0x43, v3
	v_lshl_or_b32 v5, v5, 9, v2
	ds_read_b128 v[54:57], v4
	ds_read_b128 v[50:53], v5 offset:8192
	v_min_i32_e32 v4, 51, v3
	v_lshl_or_b32 v4, v4, 9, v2
	v_min_i32_e32 v5, 35, v3
	v_lshl_or_b32 v5, v5, 9, v2
	ds_read_b128 v[46:49], v4 offset:16384
	ds_read_b128 v[42:45], v5 offset:24576
	v_min_i32_e32 v4, 19, v3
	v_lshl_or_b32 v4, v4, 9, v2
	v_min_i32_e32 v3, 3, v3
	v_lshl_or_b32 v2, v3, 9, v2
	ds_read_b128 v[38:41], v4 offset:32768
	ds_read_b128 v[34:37], v2 offset:40960
	s_lshl_b64 s[26:27], s[36:37], 17
	v_lshl_add_u64 v[2:3], v[212:213], 0, s[26:27]
	v_add_co_u32_e32 v4, vcc, s65, v2
	global_load_dwordx4 v[100:103], v[2:3], off
	global_load_dwordx4 v[92:95], v[2:3], off offset:1024
	global_load_dwordx4 v[88:91], v[2:3], off offset:2048
	global_load_dwordx4 v[80:83], v[2:3], off offset:3072
	v_addc_co_u32_e32 v5, vcc, 0, v3, vcc
	v_add_co_u32_e32 v6, vcc, s75, v2
	s_lshl_b32 s26, s36, 9
	s_nop 0
	v_addc_co_u32_e32 v7, vcc, 0, v3, vcc
	v_add_co_u32_e32 v2, vcc, s66, v2
	s_mov_b32 s27, s37
	s_nop 0
	v_addc_co_u32_e32 v3, vcc, 0, v3, vcc
	v_lshl_add_u64 v[14:15], s[26:27], 2, v[218:219]
	global_load_dwordx4 v[84:87], v[4:5], off offset:1024
	global_load_dwordx4 v[76:79], v[4:5], off offset:2048
	global_load_dwordx4 v[96:99], v[6:7], off offset:-4096
	global_load_dwordx4 v[128:131], v[6:7], off
	global_load_dwordx4 v[124:127], v[6:7], off offset:1024
	global_load_dwordx4 v[120:123], v[6:7], off offset:2048
	global_load_dwordx4 v[112:115], v[6:7], off offset:3072
	global_load_dwordx4 v[68:71], v[4:5], off offset:3072
	global_load_dwordx4 v[116:119], v[2:3], off
	global_load_dwordx4 v[108:111], v[2:3], off offset:1024
	global_load_dwordx4 v[104:107], v[2:3], off offset:2048
	global_load_dwordx4 v[72:75], v[2:3], off offset:3072
	global_load_dwordx4 v[18:21], v[14:15], off offset:1536
	global_load_dwordx4 v[22:25], v[14:15], off offset:1568
	s_nop 0
	global_load_dwordx4 v[2:5], v[14:15], off offset:1664
	global_load_dwordx4 v[6:9], v[14:15], off offset:1696
	global_load_dwordx4 v[26:29], v[14:15], off offset:1600
	global_load_dwordx4 v[30:33], v[14:15], off offset:1632
	global_load_dwordx4 v[10:13], v[14:15], off offset:1728
	s_nop 0
	global_load_dwordx4 v[14:17], v[14:15], off offset:1760
	v_mov_b32_e32 v58, v0
	s_or_b32 s80, s30, 1
	s_lshl_b32 s26, s36, 7
	s_nop 0
	v_cmp_gt_i32_e32 vcc, s76, v58
	s_and_saveexec_b64 s[30:31], vcc
	s_cbranch_execz .LBB1_126
	s_lshl_b64 s[40:41], s[26:27], 2
	s_add_u32 s40, s22, s40
	s_addc_u32 s41, s23, s41
	v_and_b32_e32 v58, 63, v0
	v_lshrrev_b32_e32 v64, 6, v0
	v_lshrrev_b32_e32 v59, 3, v58
	v_and_b32_e32 v60, 7, v58
	v_readfirstlane_b32 s52, v64
	v_min_u32_e32 v61, 4, v59
	v_lshlrev_b32_e32 v62, 6, v61
	v_lshl_add_u32 v62, v60, 3, v62
	v_mul_u32_u24_e32 v63, 7, v61
	v_add_u32_e32 v63, v63, v60
	v_cmp_gt_u32_e64 s[46:47], 5, v59
	v_cmp_gt_u32_e64 s[48:49], 7, v60
	v_cmp_gt_u32_e32 vcc, 32, v63
	v_cmp_eq_u32_e64 s[50:51], 7, v60
	s_and_b64 s[46:47], s[46:47], s[48:49]
	s_and_b64 s[46:47], s[46:47], vcc
	v_min_u32_e32 v63, 31, v63
	v_lshl_add_u32 v63, v64, 5, v63
	v_lshlrev_b32_e32 v65, 2, v63
	global_load_dword v132, v65, s[40:41]
	v_lshl_add_u32 v133, v63, 2, v249
	s_mul_i32 s52, s52, 0x140
	s_mul_i32 s53, s36, 0x5000
	s_add_i32 s53, s53, s52
	s_add_u32 s42, s18, s53
	s_addc_u32 s43, s19, 0
	s_add_u32 s44, s42, 0x1400
	s_addc_u32 s45, s43, 0
	s_mov_b32 s82, 0x10000
	s_mov_b32 s81, 0x42000000
.Lgw1_poll:
	global_load_dwordx2 v[134:135], v62, s[42:43] sc1
	global_load_dwordx2 v[136:137], v62, s[42:43] offset:1280 sc1
	global_load_dwordx2 v[138:139], v62, s[42:43] offset:2560 sc1
	global_load_dwordx2 v[140:141], v62, s[42:43] offset:3840 sc1
	global_load_dwordx2 v[142:143], v62, s[44:45] sc1
	global_load_dwordx2 v[144:145], v62, s[44:45] offset:1280 sc1
	global_load_dwordx2 v[146:147], v62, s[44:45] offset:2560 sc1
	global_load_dwordx2 v[148:149], v62, s[44:45] offset:3840 sc1
	s_waitcnt vmcnt(0)
	v_min3_f32 v150, v134, v136, v138
	v_min3_f32 v150, v150, v140, v142
	v_min3_f32 v150, v150, v144, v146
	v_min_f32_e32 v150, v150, v148
	v_cmp_eq_f32_e32 vcc, s81, v150
	s_orn2_b64 vcc, vcc, s[50:51]
	s_cmp_eq_u64 vcc, exec
	s_cbranch_scc1 .Lgw1_done
	s_sleep 1
	s_add_i32 s82, s82, -1
	s_cmp_lg_u32 s82, 0
	s_cbranch_scc1 .Lgw1_poll

.LBB1_126:
	s_or_b64 exec, exec, s[30:31]
	v_mov_b32_e32 v132, v0
	v_and_b32_e32 v134, 31, v132
	v_lshlrev_b32_e32 v58, 4, v134
	v_add_u32_e32 v59, 0x25680, v58
	v_add_u32_e32 v58, 0x25880, v58
	v_ashrrev_i32_e32 v133, 5, v132
	v_lshlrev_b32_e32 v132, 3, v134
	v_mad_u32_u24 v134, v133, s64, v132
	s_waitcnt lgkmcnt(0)
	s_barrier
	s_lshl_b64 s[2:3], s[36:37], 16
	ds_read_b128 v[62:65], v59
	ds_read_b128 v[58:61], v58
	s_waitcnt lgkmcnt(0)
	v_pk_mul_f32 v[62:63], v[62:63], v[58:59] neg_lo:[1,0] neg_hi:[1,0]
	v_pk_mul_f32 v[64:65], v[64:65], v[60:61] neg_lo:[1,0] neg_hi:[1,0]
	v_pk_fma_f32 v[54:55], v[54:55], v[58:59], v[62:63]
	v_pk_fma_f32 v[56:57], v[56:57], v[60:61], v[64:65]
	v_pk_fma_f32 v[50:51], v[50:51], v[58:59], v[62:63]
	v_pk_fma_f32 v[52:53], v[52:53], v[60:61], v[64:65]
	v_pk_fma_f32 v[46:47], v[46:47], v[58:59], v[62:63]
	v_pk_fma_f32 v[48:49], v[48:49], v[60:61], v[64:65]
	v_pk_fma_f32 v[42:43], v[42:43], v[58:59], v[62:63]
	v_pk_fma_f32 v[44:45], v[44:45], v[60:61], v[64:65]
	v_pk_fma_f32 v[38:39], v[38:39], v[58:59], v[62:63]
	v_pk_fma_f32 v[40:41], v[40:41], v[60:61], v[64:65]
	v_cvt_pk_f16_f32 v54, v54, v55
	v_cvt_pk_f16_f32 v55, v56, v57
	ds_write_b64 v134, v[54:55] offset:43008
	v_cvt_pk_f16_f32 v50, v50, v51
	v_cvt_pk_f16_f32 v51, v52, v53
	ds_write_b64 v134, v[50:51] offset:47360
	v_cvt_pk_f16_f32 v46, v46, v47
	v_cvt_pk_f16_f32 v47, v48, v49
	ds_write_b64 v134, v[46:47] offset:51712
	v_cvt_pk_f16_f32 v42, v42, v43
	v_cvt_pk_f16_f32 v43, v44, v45
	ds_write_b64 v134, v[42:43] offset:56064
	v_cvt_pk_f16_f32 v38, v38, v39
	v_cvt_pk_f16_f32 v39, v40, v41
	ds_write_b64 v134, v[38:39] offset:60416
	v_cmp_gt_i32_e32 vcc, 4, v133
	s_and_saveexec_b64 s[30:31], vcc
	v_pk_fma_f32 v[34:35], v[34:35], v[58:59], v[62:63]
	v_pk_fma_f32 v[36:37], v[36:37], v[60:61], v[64:65]
	v_cvt_pk_f16_f32 v34, v34, v35
	v_cvt_pk_f16_f32 v35, v36, v37
	ds_write_b64 v134, v[34:35] offset:64768
	s_or_b64 exec, exec, s[30:31]
	v_or_b32_e32 v34, s26, v220
	v_mov_b32_e32 v35, v66
	v_lshl_add_u64 v[34:35], v[34:35], 2, s[28:29]
	v_lshl_add_u64 v[174:175], s[2:3], 1, v[214:215]
	global_load_dword v173, v[34:35], off
	global_load_dwordx4 v[136:139], v[174:175], off
	global_load_dwordx4 v[132:135], v[174:175], off offset:1024
	v_add_u32_e32 v34, v204, v238
	s_waitcnt lgkmcnt(0)
	s_barrier
	ds_read_b128 v[168:171], v34 offset:43008
	ds_read_b128 v[164:167], v34 offset:43040
	ds_read_b128 v[160:163], v34 offset:43072
	ds_read_b128 v[156:159], v34 offset:43104
	ds_read_b128 v[152:155], v34 offset:43136
	ds_read_b128 v[148:151], v34 offset:43168
	ds_read_b128 v[144:147], v34 offset:43200
	ds_read_b128 v[140:143], v34 offset:43232
	s_mov_b32 s30, 0
	s_mov_b64 s[2:3], -1

.Lep2_end:
	v_mov_b32_e32 v2, v0
	s_waitcnt lgkmcnt(0)
	s_barrier
	s_nop 0
	v_ashrrev_i32_e32 v3, 5, v2
	v_lshlrev_b32_e32 v2, 4, v2
	v_and_b32_e32 v2, 0x1f0, v2
	v_min_i32_e32 v4, 0x53, v3
	v_lshl_or_b32 v4, v4, 9, v2
	v_min_i32_e32 v5, 0x43, v3
	v_lshl_or_b32 v5, v5, 9, v2
	ds_read_b128 v[42:45], v4
	ds_read_b128 v[38:41], v5 offset:8192
	v_min_i32_e32 v4, 51, v3
	v_lshl_or_b32 v4, v4, 9, v2
	v_min_i32_e32 v5, 35, v3
	v_lshl_or_b32 v5, v5, 9, v2
	ds_read_b128 v[34:37], v4 offset:16384
	ds_read_b128 v[30:33], v5 offset:24576
	v_min_i32_e32 v4, 19, v3
	v_lshl_or_b32 v4, v4, 9, v2
	v_min_i32_e32 v3, 3, v3
	v_lshl_or_b32 v2, v3, 9, v2
	ds_read_b128 v[22:25], v4 offset:32768
	ds_read_b128 v[18:21], v2 offset:40960
	s_add_i32 s80, s36, 1
	s_cmp_lg_u32 s36, 2
	s_cselect_b64 s[30:31], -1, 0
	s_and_b64 s[40:41], s[30:31], exec
	s_cselect_b32 s42, s80, 2
	s_lshl_b32 s40, s42, 15
	s_mov_b32 s41, s37
	v_lshl_add_u64 v[2:3], v[196:197], 0, s[40:41]
	v_lshl_add_u64 v[4:5], v[198:199], 0, s[40:41]
	v_lshl_add_u64 v[6:7], v[200:201], 0, s[40:41]
	global_load_dwordx4 v[116:119], v[2:3], off
	global_load_dwordx4 v[120:123], v[2:3], off offset:1024
	global_load_dwordx4 v[112:115], v[4:5], off
	global_load_dwordx4 v[100:103], v[4:5], off offset:1024
	global_load_dwordx4 v[96:99], v[6:7], off
	global_load_dwordx4 v[76:79], v[6:7], off offset:1024
	global_load_dwordx4 v[124:127], v[2:3], off offset:2048
	global_load_dwordx4 v[128:131], v[2:3], off offset:3072
	global_load_dwordx4 v[104:107], v[4:5], off offset:2048
	global_load_dwordx4 v[108:111], v[4:5], off offset:3072
	global_load_dwordx4 v[72:75], v[6:7], off offset:2048
	global_load_dwordx4 v[68:71], v[6:7], off offset:3072
	v_add_co_u32_e32 v2, vcc, s65, v2
	s_lshl_b32 s40, s42, 7
	s_nop 0
	v_addc_co_u32_e32 v3, vcc, 0, v3, vcc
	v_add_co_u32_e32 v4, vcc, s65, v4
	v_lshl_add_u64 v[14:15], s[40:41], 2, v[202:203]
	s_nop 0
	v_addc_co_u32_e32 v5, vcc, 0, v5, vcc
	v_add_co_u32_e32 v6, vcc, s65, v6
	s_nop 1
	v_addc_co_u32_e32 v7, vcc, 0, v7, vcc
	global_load_dwordx4 v[148:151], v[2:3], off
	global_load_dwordx4 v[152:155], v[2:3], off offset:1024
	global_load_dwordx4 v[132:135], v[4:5], off
	global_load_dwordx4 v[136:139], v[4:5], off offset:1024
	global_load_dwordx4 v[92:95], v[6:7], off
	global_load_dwordx4 v[84:87], v[6:7], off offset:1024
	global_load_dwordx4 v[156:159], v[2:3], off offset:2048
	global_load_dwordx4 v[160:163], v[2:3], off offset:3072
	global_load_dwordx4 v[140:143], v[4:5], off offset:2048
	global_load_dwordx4 v[144:147], v[4:5], off offset:3072
	global_load_dwordx4 v[88:91], v[6:7], off offset:2048
	global_load_dwordx4 v[80:83], v[6:7], off offset:3072
	s_nop 0
	global_load_dwordx4 v[2:5], v[14:15], off
	global_load_dwordx4 v[6:9], v[14:15], off offset:32
	global_load_dwordx4 v[10:13], v[14:15], off offset:64
	s_nop 0
	global_load_dwordx4 v[14:17], v[14:15], off offset:96
	s_nop 0
	global_load_dwordx4 v[26:29], v[216:217], off offset:1024
	v_mov_b32_e32 v46, v0
	s_nop 0
	v_cmp_gt_i32_e32 vcc, s76, v46
	s_and_saveexec_b64 s[40:41], vcc
	s_cbranch_execz .LBB1_207
	s_lshl_b64 s[26:27], s[26:27], 2
	s_add_u32 s26, s24, s26
	s_addc_u32 s27, s25, s27
	v_and_b32_e32 v46, 63, v0
	v_lshrrev_b32_e32 v52, 6, v0
	v_lshrrev_b32_e32 v47, 3, v46
	v_and_b32_e32 v48, 7, v46
	v_readfirstlane_b32 s52, v52
	v_min_u32_e32 v49, 4, v47
	v_lshlrev_b32_e32 v50, 6, v49
	v_lshl_add_u32 v50, v48, 3, v50
	v_mul_u32_u24_e32 v51, 7, v49
	v_add_u32_e32 v51, v51, v48
	v_cmp_gt_u32_e64 s[46:47], 5, v47
	v_cmp_gt_u32_e64 s[48:49], 7, v48
	v_cmp_gt_u32_e32 vcc, 32, v51
	v_cmp_eq_u32_e64 s[50:51], 7, v48
	s_and_b64 s[46:47], s[46:47], s[48:49]
	s_and_b64 s[46:47], s[46:47], vcc
	v_min_u32_e32 v51, 31, v51
	v_lshl_add_u32 v51, v52, 5, v51
	v_lshlrev_b32_e32 v53, 2, v51
	global_load_dword v54, v53, s[26:27]
	v_lshl_add_u32 v55, v51, 2, v249
	s_mul_i32 s52, s52, 0x140
	s_mul_i32 s53, s36, 0x5000
	s_addk_i32 s53, 0x2800
	s_add_i32 s53, s53, s52
	s_add_u32 s42, s18, s53
	s_addc_u32 s43, s19, 0
	s_add_u32 s44, s42, 0x1400
	s_addc_u32 s45, s43, 0
	s_mov_b32 s81, 0x10000
	s_mov_b32 s82, 0x42000000
.Lgw2_poll:
	global_load_dwordx2 v[56:57], v50, s[42:43] sc1
	global_load_dwordx2 v[58:59], v50, s[42:43] offset:1280 sc1
	global_load_dwordx2 v[60:61], v50, s[42:43] offset:2560 sc1
	global_load_dwordx2 v[62:63], v50, s[42:43] offset:3840 sc1
	global_load_dwordx2 v[64:65], v50, s[44:45] sc1
	global_load_dwordx2 v[164:165], v50, s[44:45] offset:1280 sc1
	global_load_dwordx2 v[166:167], v50, s[44:45] offset:2560 sc1
	global_load_dwordx2 v[168:169], v50, s[44:45] offset:3840 sc1
	s_waitcnt vmcnt(0)
	v_min3_f32 v170, v56, v58, v60
	v_min3_f32 v170, v170, v62, v64
	v_min3_f32 v170, v170, v164, v166
	v_min_f32_e32 v170, v170, v168
	v_cmp_eq_f32_e32 vcc, s82, v170
	s_orn2_b64 vcc, vcc, s[50:51]
	s_cmp_eq_u64 vcc, exec
	s_cbranch_scc1 .Lgw2_done
	s_sleep 1
	s_add_i32 s81, s81, -1
	s_cmp_lg_u32 s81, 0
	s_cbranch_scc1 .Lgw2_poll
